# v13 + barrier leader tail trim + dense-up deferred half epilogue + 64-byte K-loop alignment
# baseline (speedup 1.0000x reference)
.Lwd_g3:
	s_waitcnt lgkmcnt(0)
	s_barrier
	s_setprio 1
	s_waitcnt lgkmcnt(0)
	v_mfma_f32_16x16x128_f8f6f4 v[96:99], v[26:33], v[200:207], 0
	v_mfma_f32_16x16x128_f8f6f4 v[92:95], v[18:25], v[200:207], 0
	v_mfma_f32_16x16x128_f8f6f4 v[84:87], v[18:25], v[222:229], 0
	v_mfma_f32_16x16x128_f8f6f4 v[88:91], v[26:33], v[222:229], 0
	v_mfma_f32_16x16x128_f8f6f4 v[80:83], v[26:33], v[230:237], 0
	v_mfma_f32_16x16x128_f8f6f4 v[76:79], v[18:25], v[230:237], 0
	v_mfma_f32_16x16x128_f8f6f4 v[68:71], v[18:25], v[238:245], 0
	v_mfma_f32_16x16x128_f8f6f4 v[72:75], v[26:33], v[238:245], 0
	s_setprio 0
	s_setprio 1
	v_mfma_f32_16x16x128_f8f6f4 v[64:67], v[10:17], v[200:207], 0
	v_mfma_f32_16x16x128_f8f6f4 v[60:63], v[2:9], v[200:207], 0
	v_mfma_f32_16x16x128_f8f6f4 v[52:55], v[2:9], v[222:229], 0
	v_mfma_f32_16x16x128_f8f6f4 v[56:59], v[10:17], v[222:229], 0
	v_mfma_f32_16x16x128_f8f6f4 v[48:51], v[10:17], v[230:237], 0
	v_mfma_f32_16x16x128_f8f6f4 v[44:47], v[2:9], v[230:237], 0
	v_mfma_f32_16x16x128_f8f6f4 v[36:39], v[2:9], v[238:245], 0
	v_mfma_f32_16x16x128_f8f6f4 v[40:43], v[10:17], v[238:245], 0
	s_setprio 0
	s_barrier
	s_add_i32 s64, 0, 0x18000
	s_add_i32 s66, 0, 0x1c000
	v_add_u32_e32 v200, s64, v196
	v_add_u32_e32 v201, s66, v196
	ds_read_b128 v[26:29], v200
	ds_read_b128 v[30:33], v200 offset:1024
	ds_read_b128 v[18:21], v200 offset:2048
	ds_read_b128 v[22:25], v200 offset:3072
	ds_read_b128 v[10:13], v201
	ds_read_b128 v[14:17], v201 offset:1024
	ds_read_b128 v[2:5], v201 offset:2048
	ds_read_b128 v[6:9], v201 offset:3072
	s_add_u32 s36, s30, 0x20100
	s_addc_u32 s37, s31, 0
	s_mov_b32 m0, s43
	v_lshl_add_u64 v[178:179], s[36:37], 0, v[168:169]
	ds_read_b128 v[202:205], v197 offset:32768
	ds_read_b128 v[206:209], v197 offset:33792
	ds_read_b128 v[222:225], v197 offset:34816
	ds_read_b128 v[226:229], v197 offset:35840
	ds_read_b128 v[230:233], v197 offset:36864
	ds_read_b128 v[234:237], v197 offset:37888
	ds_read_b128 v[238:241], v197 offset:38912
	ds_read_b128 v[242:245], v197 offset:39936
	global_load_lds_dwordx4 v[178:179], off
	v_lshl_add_u64 v[178:179], s[36:37], 0, v[166:167]
	s_mov_b32 m0, s44
	s_nop 0
	global_load_lds_dwordx4 v[178:179], off
	s_waitcnt vmcnt(8)
	s_waitcnt lgkmcnt(0)
	s_barrier
	s_setprio 1
	s_waitcnt lgkmcnt(0)
	v_mfma_f32_16x16x128_f8f6f4 v[160:163], v[26:33], v[202:209], v[160:163]
	v_mfma_f32_16x16x128_f8f6f4 v[156:159], v[18:25], v[202:209], v[156:159]
	v_mfma_f32_16x16x128_f8f6f4 v[148:151], v[18:25], v[222:229], v[148:151]
	v_mfma_f32_16x16x128_f8f6f4 v[152:155], v[26:33], v[222:229], v[152:155]
	v_mfma_f32_16x16x128_f8f6f4 v[144:147], v[26:33], v[230:237], v[144:147]
	v_mfma_f32_16x16x128_f8f6f4 v[140:143], v[18:25], v[230:237], v[140:143]
	v_mfma_f32_16x16x128_f8f6f4 v[132:135], v[18:25], v[238:245], v[132:135]
	v_mfma_f32_16x16x128_f8f6f4 v[136:139], v[26:33], v[238:245], v[136:139]
	s_setprio 0
	s_setprio 1
	v_mfma_f32_16x16x128_f8f6f4 v[128:131], v[10:17], v[202:209], v[128:131]
	v_mfma_f32_16x16x128_f8f6f4 v[124:127], v[2:9], v[202:209], v[124:127]
	v_mfma_f32_16x16x128_f8f6f4 v[116:119], v[2:9], v[222:229], v[116:119]
	v_mfma_f32_16x16x128_f8f6f4 v[120:123], v[10:17], v[222:229], v[120:123]
	v_mfma_f32_16x16x128_f8f6f4 v[112:115], v[10:17], v[230:237], v[112:115]
	v_mfma_f32_16x16x128_f8f6f4 v[108:111], v[2:9], v[230:237], v[108:111]
	v_mfma_f32_16x16x128_f8f6f4 v[100:103], v[2:9], v[238:245], v[100:103]
	v_mfma_f32_16x16x128_f8f6f4 v[104:107], v[10:17], v[238:245], v[104:107]
	s_setprio 0
	s_barrier
	s_add_i32 s64, s64, s40
	s_mov_b64 s[24:25], 0x180
	s_add_i32 s65, s64, 0x2000
	v_lshl_add_u64 v[174:175], v[174:175], 0, s[24:25]
	s_mov_b32 m0, s64
	s_add_u32 s36, s22, 0x20180
	ds_read_b128 v[202:205], v197 offset:49152
	ds_read_b128 v[206:209], v197 offset:50176
	ds_read_b128 v[222:225], v197 offset:51200
	ds_read_b128 v[226:229], v197 offset:52224
	ds_read_b128 v[230:233], v197 offset:53248
	ds_read_b128 v[234:237], v197 offset:54272
	ds_read_b128 v[238:241], v197 offset:55296
	ds_read_b128 v[242:245], v197 offset:56320
	global_load_lds_dwordx4 v[174:175], off
	v_lshl_add_u64 v[174:175], v[190:191], 0, s[24:25]
	s_mov_b32 m0, s65
	s_addc_u32 s37, s23, 0
	s_add_i32 s66, s66, s40
	global_load_lds_dwordx4 v[174:175], off
	v_lshl_add_u64 v[174:175], s[36:37], 0, v[34:35]
	s_mov_b32 m0, s66
	s_add_i32 s67, s66, 0x2000
	global_load_lds_dwordx4 v[174:175], off
	v_lshl_add_u64 v[174:175], s[36:37], 0, v[164:165]
	s_mov_b32 m0, s67
	s_nop 0
	global_load_lds_dwordx4 v[174:175], off
	v_lshl_add_u64 v[174:175], v[192:193], 0, s[24:25]
	s_mov_b32 m0, s47
	s_nop 0
	global_load_lds_dwordx4 v[174:175], off
	v_lshl_add_u64 v[174:175], v[194:195], 0, s[24:25]
	s_mov_b32 m0, s48
	s_nop 0
	global_load_lds_dwordx4 v[174:175], off
	s_waitcnt vmcnt(8)
	s_waitcnt lgkmcnt(0)
	s_barrier
	s_setprio 1
	s_waitcnt lgkmcnt(0)
	v_mfma_f32_16x16x128_f8f6f4 v[96:99], v[26:33], v[202:209], v[96:99]
	v_mfma_f32_16x16x128_f8f6f4 v[92:95], v[18:25], v[202:209], v[92:95]
	v_mfma_f32_16x16x128_f8f6f4 v[84:87], v[18:25], v[222:229], v[84:87]
	v_mfma_f32_16x16x128_f8f6f4 v[88:91], v[26:33], v[222:229], v[88:91]
	v_mfma_f32_16x16x128_f8f6f4 v[80:83], v[26:33], v[230:237], v[80:83]
	v_mfma_f32_16x16x128_f8f6f4 v[76:79], v[18:25], v[230:237], v[76:79]
	v_mfma_f32_16x16x128_f8f6f4 v[68:71], v[18:25], v[238:245], v[68:71]
	v_mfma_f32_16x16x128_f8f6f4 v[72:75], v[26:33], v[238:245], v[72:75]
	s_setprio 0
	s_setprio 1
	v_mfma_f32_16x16x128_f8f6f4 v[64:67], v[10:17], v[202:209], v[64:67]
	v_mfma_f32_16x16x128_f8f6f4 v[60:63], v[2:9], v[202:209], v[60:63]
	v_mfma_f32_16x16x128_f8f6f4 v[52:55], v[2:9], v[222:229], v[52:55]
	v_mfma_f32_16x16x128_f8f6f4 v[56:59], v[10:17], v[222:229], v[56:59]
	v_mfma_f32_16x16x128_f8f6f4 v[48:51], v[10:17], v[230:237], v[48:51]
	v_mfma_f32_16x16x128_f8f6f4 v[44:47], v[2:9], v[230:237], v[44:47]
	v_mfma_f32_16x16x128_f8f6f4 v[36:39], v[2:9], v[238:245], v[36:39]
	v_mfma_f32_16x16x128_f8f6f4 v[40:43], v[10:17], v[238:245], v[40:43]
	s_setprio 0
	s_barrier
	s_add_u32 s30, s30, 0x20180
	s_addc_u32 s31, s31, 0
	s_add_u32 s68, s22, 0x200
	s_addc_u32 s69, s23, 0
	s_mov_b32 s70, 0
	.p2align	6
